# v045 + NA phase: the 64 ctx attention units run on wave 0 of workgroups 8..71 instead of all waves of workgroups 0..7
# speedup vs baseline: 1.0204x; 1.0193x over previous
; __device__ __forceinline__ unsigned cvt_pk_bf16(float lo, float hi) { const f32x2 v = {lo, hi}; const bf16v2_t r = __builtin_convertvector(v, bf16v2_t); return __builtin_bit_cast(unsigned, r); }
; __device__ __forceinline__ void lds_fence() { asm volatile("s_waitcnt lgkmcnt(0)" ::: "memory"); }
; __device__ __forceinline__ void ph_na2(const int vc, const Params& p, LAS unsigned char* lds) {
;     ...
;     for (int it = vc * 8 + w; it < 2048 + 64; it += gridDim.x * 8) {
;         const bool lat = it < 2048;
;         int b, h, i = 0, qrow0;
;         if (lat) { b = it >> 10; h = (it >> 7) & 7; i = it & 127; qrow0 = b * SEQ + i * 64; }
;         else { const int q = it - 2048; b = q >> 5; h = (q >> 2) & 7; qrow0 = ML + b * CTX + (q & 3) * 64; }
;     ...
; #pragma unroll
;         for (int qb = 0; qb < 2; ++qb) { const float inv = 1.f / l_run[qb]; bf16_t* orow = AB + (size_t)(qrow0 + 32 * qb + lc) * D + h * 64 + 4 * lh;
; #pragma unroll
;             for (int db = 0; db < 2; ++db)
; #pragma unroll
;                 for (int g = 0; g < 4; ++g) { u32x2 wv; wv.x = cvt_pk_bf16(O[qb][db][4 * g] * inv, O[qb][db][4 * g + 1] * inv); wv.y = cvt_pk_bf16(O[qb][db][4 * g + 2] * inv, O[qb][db][4 * g + 3] * inv);
;                     *(u32x2*)(orow + 32 * db + 8 * g) = wv; } }
;         lds_fence();
.LBB0_284:
	s_or_b64 exec, exec, s[6:7]
	v_div_scale_f32 v69, s[4:5], v221, v221, 1.0
	v_rcp_f32_e32 v72, v69
	v_lshlrev_b32_e32 v2, 7, v214
	v_lshl_add_u64 v[70:71], v[196:197], 0, v[2:3]
	v_add_u32_e32 v68, v213, v189
	v_fma_f32 v2, -v69, v72, 1.0
	v_fmac_f32_e32 v72, v2, v72
	v_div_scale_f32 v2, vcc, 1.0, v221, 1.0
	v_mul_f32_e32 v73, v2, v72
	v_fma_f32 v74, -v69, v73, v2
	v_fmac_f32_e32 v73, v74, v72
	v_fma_f32 v2, -v69, v73, v2
	v_div_fmas_f32 v2, v2, v72, v73
	v_div_fixup_f32 v2, v2, v221, 1.0
	v_ashrrev_i32_e32 v69, 31, v68
	v_lshlrev_b64 v[72:73], 11, v[68:69]
	v_pk_mul_f32 v[36:37], v[2:3], v[36:37] op_sel_hi:[0,1]
	v_pk_mul_f32 v[38:39], v[2:3], v[38:39] op_sel_hi:[0,1]
	v_lshl_add_u64 v[72:73], v[70:71], 0, v[72:73]
	v_pk_mul_f32 v[52:53], v[2:3], v[52:53] op_sel_hi:[0,1]
	v_pk_mul_f32 v[54:55], v[2:3], v[54:55] op_sel_hi:[0,1]
	v_cvt_pk_bf16_f32 v36, v36, v37
	v_cvt_pk_bf16_f32 v37, v38, v39
	v_cvt_pk_bf16_f32 v52, v52, v53
	v_cvt_pk_bf16_f32 v53, v54, v55
	global_store_dwordx2 v[72:73], v[36:37], off offset:64
	v_pk_mul_f32 v[36:37], v[2:3], v[40:41] op_sel_hi:[0,1]
	v_div_scale_f32 v40, s[4:5], v224, v224, 1.0
	global_store_dwordx2 v[72:73], v[52:53], off
	v_pk_mul_f32 v[52:53], v[2:3], v[56:57] op_sel_hi:[0,1]
	v_pk_mul_f32 v[54:55], v[2:3], v[58:59] op_sel_hi:[0,1]
	v_pk_mul_f32 v[38:39], v[2:3], v[42:43] op_sel_hi:[0,1]
	v_rcp_f32_e32 v41, v40
	v_cvt_pk_bf16_f32 v52, v52, v53
	v_cvt_pk_bf16_f32 v53, v54, v55
	v_cvt_pk_bf16_f32 v36, v36, v37
	v_cvt_pk_bf16_f32 v37, v38, v39
	global_store_dwordx2 v[72:73], v[52:53], off offset:16
	v_pk_mul_f32 v[52:53], v[2:3], v[60:61] op_sel_hi:[0,1]
	v_pk_mul_f32 v[54:55], v[2:3], v[62:63] op_sel_hi:[0,1]
	global_store_dwordx2 v[72:73], v[36:37], off offset:80
	v_pk_mul_f32 v[36:37], v[2:3], v[44:45] op_sel_hi:[0,1]
	v_pk_mul_f32 v[38:39], v[2:3], v[46:47] op_sel_hi:[0,1]
	v_cvt_pk_bf16_f32 v52, v52, v53
	v_cvt_pk_bf16_f32 v53, v54, v55
	v_cvt_pk_bf16_f32 v36, v36, v37
	v_cvt_pk_bf16_f32 v37, v38, v39
	global_store_dwordx2 v[72:73], v[52:53], off offset:32
	v_pk_mul_f32 v[52:53], v[2:3], v[64:65] op_sel_hi:[0,1]
	v_pk_mul_f32 v[54:55], v[2:3], v[66:67] op_sel_hi:[0,1]
	global_store_dwordx2 v[72:73], v[36:37], off offset:96
	v_pk_mul_f32 v[36:37], v[2:3], v[48:49] op_sel_hi:[0,1]
	v_pk_mul_f32 v[38:39], v[2:3], v[50:51] op_sel_hi:[0,1]
	v_fma_f32 v2, -v40, v41, 1.0
	v_cvt_pk_bf16_f32 v36, v36, v37
	v_cvt_pk_bf16_f32 v37, v38, v39
	v_fmac_f32_e32 v41, v2, v41
	v_div_scale_f32 v2, vcc, 1.0, v224, 1.0
	global_store_dwordx2 v[72:73], v[36:37], off offset:112
	v_mul_f32_e32 v36, v2, v41
	v_fma_f32 v37, -v40, v36, v2
	v_fmac_f32_e32 v36, v37, v41
	v_fma_f32 v2, -v40, v36, v2
	v_div_fmas_f32 v2, v2, v41, v36
	v_add_u32_e32 v36, 32, v68
	v_div_fixup_f32 v2, v2, v224, 1.0
	v_ashrrev_i32_e32 v37, 31, v36
	v_lshlrev_b64 v[36:37], 11, v[36:37]
	v_pk_mul_f32 v[20:21], v[2:3], v[20:21] op_sel_hi:[0,1]
	v_pk_mul_f32 v[22:23], v[2:3], v[22:23] op_sel_hi:[0,1]
	v_pk_mul_f32 v[4:5], v[2:3], v[4:5] op_sel_hi:[0,1]
	v_pk_mul_f32 v[6:7], v[2:3], v[6:7] op_sel_hi:[0,1]
	v_lshl_add_u64 v[36:37], v[70:71], 0, v[36:37]
	v_cvt_pk_bf16_f32 v20, v20, v21
	v_cvt_pk_bf16_f32 v21, v22, v23
	v_cvt_pk_bf16_f32 v4, v4, v5
	v_cvt_pk_bf16_f32 v5, v6, v7
	global_store_dwordx2 v[36:37], v[20:21], off
	v_pk_mul_f32 v[20:21], v[2:3], v[24:25] op_sel_hi:[0,1]
	v_pk_mul_f32 v[22:23], v[2:3], v[26:27] op_sel_hi:[0,1]
	global_store_dwordx2 v[36:37], v[4:5], off offset:64
	v_pk_mul_f32 v[4:5], v[2:3], v[8:9] op_sel_hi:[0,1]
	v_pk_mul_f32 v[6:7], v[2:3], v[10:11] op_sel_hi:[0,1]
	v_cvt_pk_bf16_f32 v20, v20, v21
	v_cvt_pk_bf16_f32 v21, v22, v23
	v_cvt_pk_bf16_f32 v4, v4, v5
	v_cvt_pk_bf16_f32 v5, v6, v7
	global_store_dwordx2 v[36:37], v[20:21], off offset:16
	v_pk_mul_f32 v[20:21], v[2:3], v[28:29] op_sel_hi:[0,1]
	v_pk_mul_f32 v[22:23], v[2:3], v[30:31] op_sel_hi:[0,1]
	global_store_dwordx2 v[36:37], v[4:5], off offset:80
	v_pk_mul_f32 v[4:5], v[2:3], v[12:13] op_sel_hi:[0,1]
	v_pk_mul_f32 v[6:7], v[2:3], v[14:15] op_sel_hi:[0,1]
	v_cvt_pk_bf16_f32 v20, v20, v21
	v_cvt_pk_bf16_f32 v21, v22, v23
	v_cvt_pk_bf16_f32 v4, v4, v5
	v_cvt_pk_bf16_f32 v5, v6, v7
	global_store_dwordx2 v[36:37], v[20:21], off offset:32
	v_pk_mul_f32 v[20:21], v[2:3], v[32:33] op_sel_hi:[0,1]
	v_pk_mul_f32 v[22:23], v[2:3], v[34:35] op_sel_hi:[0,1]
	global_store_dwordx2 v[36:37], v[4:5], off offset:96
	v_pk_mul_f32 v[4:5], v[2:3], v[16:17] op_sel_hi:[0,1]
	v_pk_mul_f32 v[6:7], v[2:3], v[18:19] op_sel_hi:[0,1]
	v_cvt_pk_bf16_f32 v52, v52, v53
	v_cvt_pk_bf16_f32 v53, v54, v55
	v_cvt_pk_bf16_f32 v20, v20, v21
	v_cvt_pk_bf16_f32 v21, v22, v23
	v_cvt_pk_bf16_f32 v4, v4, v5
	v_cvt_pk_bf16_f32 v5, v6, v7
	global_store_dwordx2 v[72:73], v[52:53], off offset:48
	global_store_dwordx2 v[36:37], v[20:21], off offset:48
	global_store_dwordx2 v[36:37], v[4:5], off offset:112
	v_readlane_b32 s4, v250, 28
	s_waitcnt lgkmcnt(0)
	v_readlane_b32 s5, v250, 29
	s_nop 0
	v_and_b32_e32 v6, 7, v1
	v_lshrrev_b32_e32 v7, 3, v1
	v_subrev_u32_e32 v7, 8, v7
	v_cmp_gt_u32_e32 vcc, 64, v7
	v_cmp_eq_u32_e64 s[6:7], 0, v6
	s_and_b64 vcc, vcc, s[6:7]
	v_cmp_gt_i32_e64 s[6:7], s24, v1
	s_and_b64 vcc, vcc, s[6:7]
	v_add_u32_e32 v7, 0x800, v7
	v_mov_b32_e32 v6, 0x1000
	v_cndmask_b32_e32 v1, v6, v7, vcc
	v_cmp_lt_i32_e32 vcc, s30, v1
	s_or_b64 s[16:17], vcc, s[16:17]
	s_andn2_b64 exec, exec, s[16:17]
	s_cbranch_execz .LBB0_389
